# expert-down GEMM: row gates requested at the unit's K-loop start instead of load+wait in the epilogue (on top of v23)
# speedup vs baseline: 1.0051x; 1.0051x over previous
.LBB0_1840:
	s_ashr_i32 s31, s30, 31
	s_lshl_b64 s[14:15], s[30:31], 19
	s_add_u32 s48, s40, s14
	s_addc_u32 s49, s41, s15
	s_and_b64 s[14:15], s[58:59], exec
	s_cselect_b32 s9, s49, s57
	s_cselect_b32 s14, s48, s56
	s_ashr_i32 s35, s34, 31
	s_lshl_b64 s[50:51], s[34:35], 19
	s_add_u32 s50, s63, s50
	s_addc_u32 s51, s64, s51
	s_and_b64 s[58:59], s[58:59], exec
	s_cselect_b32 s15, s51, s55
	s_cselect_b32 s31, s50, s54
	s_add_u32 s35, s54, 0x100
	s_addc_u32 s86, s55, 0
	s_add_u32 s54, s56, 0x40080
	v_mov_b32_e32 v2, 0
	s_addc_u32 s55, s57, 0
	s_mov_b32 s87, -2
	v_mov_b32_e32 v3, v2
	v_mov_b32_e32 v4, v2
	v_mov_b32_e32 v5, v2
	v_mov_b32_e32 v6, v2
	v_mov_b32_e32 v7, v2
	v_mov_b32_e32 v8, v2
	v_mov_b32_e32 v9, v2
	v_mov_b32_e32 v14, v2
	v_mov_b32_e32 v15, v2
	v_mov_b32_e32 v16, v2
	v_mov_b32_e32 v17, v2
	v_mov_b32_e32 v22, v2
	v_mov_b32_e32 v23, v2
	v_mov_b32_e32 v24, v2
	v_mov_b32_e32 v25, v2
	v_mov_b32_e32 v30, v2
	v_mov_b32_e32 v31, v2
	v_mov_b32_e32 v32, v2
	v_mov_b32_e32 v33, v2
	v_mov_b32_e32 v38, v2
	v_mov_b32_e32 v39, v2
	v_mov_b32_e32 v40, v2
	v_mov_b32_e32 v41, v2
	v_mov_b32_e32 v46, v2
	v_mov_b32_e32 v47, v2
	v_mov_b32_e32 v48, v2
	v_mov_b32_e32 v49, v2
	v_mov_b32_e32 v54, v2
	v_mov_b32_e32 v55, v2
	v_mov_b32_e32 v56, v2
	v_mov_b32_e32 v57, v2
	v_mov_b32_e32 v10, v2
	v_mov_b32_e32 v11, v2
	v_mov_b32_e32 v12, v2
	v_mov_b32_e32 v13, v2
	v_mov_b32_e32 v18, v2
	v_mov_b32_e32 v19, v2
	v_mov_b32_e32 v20, v2
	v_mov_b32_e32 v21, v2
	v_mov_b32_e32 v26, v2
	v_mov_b32_e32 v27, v2
	v_mov_b32_e32 v28, v2
	v_mov_b32_e32 v29, v2
	v_mov_b32_e32 v34, v2
	v_mov_b32_e32 v35, v2
	v_mov_b32_e32 v36, v2
	v_mov_b32_e32 v37, v2
	v_mov_b32_e32 v42, v2
	v_mov_b32_e32 v43, v2
	v_mov_b32_e32 v44, v2
	v_mov_b32_e32 v45, v2
	v_mov_b32_e32 v50, v2
	v_mov_b32_e32 v51, v2
	v_mov_b32_e32 v52, v2
	v_mov_b32_e32 v53, v2
	v_mov_b32_e32 v58, v2
	v_mov_b32_e32 v59, v2
	v_mov_b32_e32 v60, v2
	v_mov_b32_e32 v61, v2
	v_mov_b32_e32 v62, v2
	v_mov_b32_e32 v63, v2
	v_mov_b32_e32 v64, v2
	v_mov_b32_e32 v65, v2
	v_mov_b32_e32 v66, v2
	v_mov_b32_e32 v67, v2
	v_mov_b32_e32 v68, v2
	v_mov_b32_e32 v69, v2
	v_mov_b32_e32 v70, v2
	v_mov_b32_e32 v71, v2
	v_mov_b32_e32 v72, v2
	v_mov_b32_e32 v73, v2
	v_mov_b32_e32 v82, v2
	v_mov_b32_e32 v83, v2
	v_mov_b32_e32 v84, v2
	v_mov_b32_e32 v85, v2
	v_mov_b32_e32 v86, v2
	v_mov_b32_e32 v87, v2
	v_mov_b32_e32 v88, v2
	v_mov_b32_e32 v89, v2
	v_mov_b32_e32 v98, v2
	v_mov_b32_e32 v99, v2
	v_mov_b32_e32 v100, v2
	v_mov_b32_e32 v101, v2
	v_mov_b32_e32 v102, v2
	v_mov_b32_e32 v103, v2
	v_mov_b32_e32 v104, v2
	v_mov_b32_e32 v105, v2
	v_mov_b32_e32 v114, v2
	v_mov_b32_e32 v115, v2
	v_mov_b32_e32 v116, v2
	v_mov_b32_e32 v117, v2
	v_mov_b32_e32 v118, v2
	v_mov_b32_e32 v119, v2
	v_mov_b32_e32 v120, v2
	v_mov_b32_e32 v121, v2
	v_mov_b32_e32 v74, v2
	v_mov_b32_e32 v75, v2
	v_mov_b32_e32 v76, v2
	v_mov_b32_e32 v77, v2
	v_mov_b32_e32 v78, v2
	v_mov_b32_e32 v79, v2
	v_mov_b32_e32 v80, v2
	v_mov_b32_e32 v81, v2
	v_mov_b32_e32 v90, v2
	v_mov_b32_e32 v91, v2
	v_mov_b32_e32 v92, v2
	v_mov_b32_e32 v93, v2
	v_mov_b32_e32 v94, v2
	v_mov_b32_e32 v95, v2
	v_mov_b32_e32 v96, v2
	v_mov_b32_e32 v97, v2
	v_mov_b32_e32 v106, v2
	v_mov_b32_e32 v107, v2
	v_mov_b32_e32 v108, v2
	v_mov_b32_e32 v109, v2
	v_mov_b32_e32 v110, v2
	v_mov_b32_e32 v111, v2
	v_mov_b32_e32 v112, v2
	v_mov_b32_e32 v113, v2
	v_mov_b32_e32 v122, v2
	v_mov_b32_e32 v123, v2
	v_mov_b32_e32 v124, v2
	v_mov_b32_e32 v125, v2
	v_mov_b32_e32 v126, v2
	v_mov_b32_e32 v127, v2
	v_mov_b32_e32 v128, v2
	v_mov_b32_e32 v129, v2
	v_lshl_add_u32 v248, s38, 8, v143
	v_ashrrev_i32_e32 v249, 31, v248
	v_lshl_add_u64 v[248:249], v[248:249], 2, s[44:45]
	global_load_dword v240, v[248:249], off
	global_load_dword v241, v[248:249], off offset:64
	global_load_dword v242, v[248:249], off offset:128
	global_load_dword v243, v[248:249], off offset:192
	global_load_dword v244, v[248:249], off offset:512
	global_load_dword v245, v[248:249], off offset:576
	global_load_dword v246, v[248:249], off offset:640
	global_load_dword v247, v[248:249], off offset:704
.LBB0_1841:
	s_add_u32 s56, s54, 0xfffc0080
	s_addc_u32 s57, s55, -1
	s_add_i32 s96, 0, 0x10040
	v_add_u32_e32 v142, s96, v145
	ds_read_b128 v[150:153], v142
	ds_read_b128 v[154:157], v142 offset:1024
	ds_read_b128 v[158:161], v142 offset:2048
	ds_read_b128 v[162:165], v142 offset:3072
	s_cmp_eq_u32 s87, 12
	s_cselect_b32 s59, s9, s57
	s_cselect_b32 s58, s14, s56
	s_cselect_b32 s57, s15, s86
	s_cselect_b32 s56, s31, s35
	v_lshl_add_u64 v[196:197], s[54:55], 0, v[140:141]
	s_add_i32 m0, s39, 0xc040
	ds_read_b128 v[166:169], v149 offset:64
	ds_read_b128 v[170:173], v149 offset:1088
	ds_read_b128 v[174:177], v149 offset:2112
	ds_read_b128 v[178:181], v149 offset:3136
	ds_read_b128 v[182:185], v149 offset:4160
	ds_read_b128 v[186:189], v149 offset:5184
	ds_read_b128 v[190:193], v149 offset:6208
	ds_read_b128 v[198:201], v149 offset:7232
	global_load_lds_dwordx4 v[196:197], off
	v_lshl_add_u64 v[196:197], s[54:55], 0, v[138:139]
	s_add_i32 m0, s39, 0xe040
	s_nop 0
	global_load_lds_dwordx4 v[196:197], off
	s_waitcnt lgkmcnt(8)
	s_barrier
	s_waitcnt lgkmcnt(0)
	s_setprio 1
	s_waitcnt lgkmcnt(0)
	v_mfma_f32_16x16x32_bf16 v[126:129], v[150:153], v[166:169], v[126:129]
	v_mfma_f32_16x16x32_bf16 v[122:125], v[158:161], v[166:169], v[122:125]
	v_mfma_f32_16x16x32_bf16 v[110:113], v[150:153], v[174:177], v[110:113]
	v_mfma_f32_16x16x32_bf16 v[106:109], v[158:161], v[174:177], v[106:109]
	v_mfma_f32_16x16x32_bf16 v[94:97], v[150:153], v[182:185], v[94:97]
	v_mfma_f32_16x16x32_bf16 v[90:93], v[158:161], v[182:185], v[90:93]
	v_mfma_f32_16x16x32_bf16 v[78:81], v[150:153], v[190:193], v[78:81]
	v_mfma_f32_16x16x32_bf16 v[74:77], v[158:161], v[190:193], v[74:77]
	v_mfma_f32_16x16x32_bf16 v[126:129], v[154:157], v[170:173], v[126:129]
	v_mfma_f32_16x16x32_bf16 v[122:125], v[162:165], v[170:173], v[122:125]
	v_mfma_f32_16x16x32_bf16 v[110:113], v[154:157], v[178:181], v[110:113]
	v_mfma_f32_16x16x32_bf16 v[106:109], v[162:165], v[178:181], v[106:109]
	v_mfma_f32_16x16x32_bf16 v[94:97], v[154:157], v[186:189], v[94:97]
	v_mfma_f32_16x16x32_bf16 v[90:93], v[162:165], v[186:189], v[90:93]
	v_mfma_f32_16x16x32_bf16 v[78:81], v[154:157], v[198:201], v[78:81]
	v_mfma_f32_16x16x32_bf16 v[74:77], v[162:165], v[198:201], v[74:77]
	s_setprio 0
	s_barrier
	s_add_i32 vcc_lo, 0, 0x14040
	s_add_i32 s96, s96, s65
	v_add_u32_e32 v142, vcc_lo, v145
	v_lshl_add_u64 v[196:197], s[56:57], 0, v[132:133]
	s_mov_b32 m0, s96
	ds_read_b128 v[202:205], v142
	ds_read_b128 v[206:209], v142 offset:1024
	ds_read_b128 v[210:213], v142 offset:2048
	ds_read_b128 v[214:217], v142 offset:3072
	global_load_lds_dwordx4 v[196:197], off
	v_lshl_add_u64 v[218:219], s[56:57], 0, v[136:137]
	s_add_i32 m0, s96, 0x2000
	s_nop 0
	global_load_lds_dwordx4 v[218:219], off
	s_barrier
	s_waitcnt lgkmcnt(0)
	s_setprio 1
	s_waitcnt lgkmcnt(0)
	v_mfma_f32_16x16x32_bf16 v[118:121], v[202:205], v[166:169], v[118:121]
	v_mfma_f32_16x16x32_bf16 v[114:117], v[210:213], v[166:169], v[114:117]
	v_mfma_f32_16x16x32_bf16 v[102:105], v[202:205], v[174:177], v[102:105]
	v_mfma_f32_16x16x32_bf16 v[98:101], v[210:213], v[174:177], v[98:101]
	v_mfma_f32_16x16x32_bf16 v[86:89], v[202:205], v[182:185], v[86:89]
	v_mfma_f32_16x16x32_bf16 v[82:85], v[210:213], v[182:185], v[82:85]
	v_mfma_f32_16x16x32_bf16 v[70:73], v[202:205], v[190:193], v[70:73]
	v_mfma_f32_16x16x32_bf16 v[66:69], v[210:213], v[190:193], v[66:69]
	v_mfma_f32_16x16x32_bf16 v[118:121], v[206:209], v[170:173], v[118:121]
	v_mfma_f32_16x16x32_bf16 v[114:117], v[214:217], v[170:173], v[114:117]
	v_mfma_f32_16x16x32_bf16 v[102:105], v[206:209], v[178:181], v[102:105]
	v_mfma_f32_16x16x32_bf16 v[98:101], v[214:217], v[178:181], v[98:101]
	v_mfma_f32_16x16x32_bf16 v[86:89], v[206:209], v[186:189], v[86:89]
	v_mfma_f32_16x16x32_bf16 v[82:85], v[214:217], v[186:189], v[82:85]
	v_mfma_f32_16x16x32_bf16 v[70:73], v[206:209], v[198:201], v[70:73]
	v_mfma_f32_16x16x32_bf16 v[66:69], v[214:217], v[198:201], v[66:69]
	s_setprio 0
	s_mov_b32 m0, s53
	v_lshl_add_u64 v[222:223], s[58:59], 0, v[130:131]
	s_barrier
	ds_read_b128 v[166:169], v149 offset:16448
	ds_read_b128 v[170:173], v149 offset:17472
	ds_read_b128 v[174:177], v149 offset:18496
	ds_read_b128 v[178:181], v149 offset:19520
	ds_read_b128 v[182:185], v149 offset:20544
	ds_read_b128 v[186:189], v149 offset:21568
	ds_read_b128 v[190:193], v149 offset:22592
	ds_read_b128 v[198:201], v149 offset:23616
	global_load_lds_dwordx4 v[222:223], off
	v_lshl_add_u64 v[224:225], s[58:59], 0, v[134:135]
	s_mov_b32 m0, s66
	s_nop 0
	global_load_lds_dwordx4 v[224:225], off
	s_barrier
	s_waitcnt lgkmcnt(0)
	s_setprio 1
	s_waitcnt lgkmcnt(0)
	v_mfma_f32_16x16x32_bf16 v[62:65], v[150:153], v[166:169], v[62:65]
	v_mfma_f32_16x16x32_bf16 v[58:61], v[158:161], v[166:169], v[58:61]
	v_mfma_f32_16x16x32_bf16 v[50:53], v[150:153], v[174:177], v[50:53]
	v_mfma_f32_16x16x32_bf16 v[42:45], v[158:161], v[174:177], v[42:45]
	v_mfma_f32_16x16x32_bf16 v[34:37], v[150:153], v[182:185], v[34:37]
	v_mfma_f32_16x16x32_bf16 v[26:29], v[158:161], v[182:185], v[26:29]
	v_mfma_f32_16x16x32_bf16 v[18:21], v[150:153], v[190:193], v[18:21]
	v_mfma_f32_16x16x32_bf16 v[10:13], v[158:161], v[190:193], v[10:13]
	v_mfma_f32_16x16x32_bf16 v[62:65], v[154:157], v[170:173], v[62:65]
	v_mfma_f32_16x16x32_bf16 v[58:61], v[162:165], v[170:173], v[58:61]
	v_mfma_f32_16x16x32_bf16 v[50:53], v[154:157], v[178:181], v[50:53]
	v_mfma_f32_16x16x32_bf16 v[42:45], v[162:165], v[178:181], v[42:45]
	v_mfma_f32_16x16x32_bf16 v[34:37], v[154:157], v[186:189], v[34:37]
	v_mfma_f32_16x16x32_bf16 v[26:29], v[162:165], v[186:189], v[26:29]
	v_mfma_f32_16x16x32_bf16 v[18:21], v[154:157], v[198:201], v[18:21]
	v_mfma_f32_16x16x32_bf16 v[10:13], v[162:165], v[198:201], v[10:13]
	s_setprio 0
	s_barrier
	s_add_u32 s96, s56, 0x40000
	s_addc_u32 s97, s57, 0
	s_add_i32 vcc_lo, vcc_lo, s65
	v_lshl_add_u64 v[150:151], s[96:97], 0, v[132:133]
	s_mov_b32 m0, vcc_lo
	s_nop 0
	global_load_lds_dwordx4 v[150:151], off
	v_lshl_add_u64 v[150:151], s[96:97], 0, v[136:137]
	s_add_i32 m0, vcc_lo, 0x2000
	s_nop 0
	global_load_lds_dwordx4 v[150:151], off
	s_waitcnt vmcnt(6)
	s_barrier
	s_setprio 1
	v_mfma_f32_16x16x32_bf16 v[54:57], v[202:205], v[166:169], v[54:57]
	v_mfma_f32_16x16x32_bf16 v[46:49], v[210:213], v[166:169], v[46:49]
	v_mfma_f32_16x16x32_bf16 v[38:41], v[202:205], v[174:177], v[38:41]
	v_mfma_f32_16x16x32_bf16 v[30:33], v[210:213], v[174:177], v[30:33]
	v_mfma_f32_16x16x32_bf16 v[22:25], v[202:205], v[182:185], v[22:25]
	v_mfma_f32_16x16x32_bf16 v[14:17], v[210:213], v[182:185], v[14:17]
	v_mfma_f32_16x16x32_bf16 v[6:9], v[202:205], v[190:193], v[6:9]
	v_mfma_f32_16x16x32_bf16 v[2:5], v[210:213], v[190:193], v[2:5]
	v_mfma_f32_16x16x32_bf16 v[54:57], v[206:209], v[170:173], v[54:57]
	v_mfma_f32_16x16x32_bf16 v[46:49], v[214:217], v[170:173], v[46:49]
	v_mfma_f32_16x16x32_bf16 v[38:41], v[206:209], v[178:181], v[38:41]
	v_mfma_f32_16x16x32_bf16 v[30:33], v[214:217], v[178:181], v[30:33]
	v_mfma_f32_16x16x32_bf16 v[22:25], v[206:209], v[186:189], v[22:25]
	v_mfma_f32_16x16x32_bf16 v[14:17], v[214:217], v[186:189], v[14:17]
	v_mfma_f32_16x16x32_bf16 v[6:9], v[206:209], v[198:201], v[6:9]
	v_mfma_f32_16x16x32_bf16 v[2:5], v[214:217], v[198:201], v[2:5]
	s_setprio 0
	s_add_i32 s96, 0, 0x18040
	v_add_u32_e32 v142, s96, v145
	s_barrier
	ds_read_b128 v[150:153], v142
	ds_read_b128 v[154:157], v142 offset:1024
	ds_read_b128 v[158:161], v142 offset:2048
	ds_read_b128 v[162:165], v142 offset:3072
	s_add_u32 s58, s58, 0x40000
	s_addc_u32 s59, s59, 0
	s_mov_b32 m0, s67
	v_lshl_add_u64 v[202:203], s[58:59], 0, v[130:131]
	ds_read_b128 v[166:169], v149 offset:32832
	ds_read_b128 v[170:173], v149 offset:33856
	ds_read_b128 v[174:177], v149 offset:34880
	ds_read_b128 v[178:181], v149 offset:35904
	ds_read_b128 v[182:185], v149 offset:36928
	ds_read_b128 v[186:189], v149 offset:37952
	ds_read_b128 v[190:193], v149 offset:38976
	ds_read_b128 v[198:201], v149 offset:40000
	global_load_lds_dwordx4 v[202:203], off
	v_lshl_add_u64 v[202:203], s[58:59], 0, v[134:135]
	s_mov_b32 m0, s68
	s_nop 0
	global_load_lds_dwordx4 v[202:203], off
	s_waitcnt lgkmcnt(8)
	s_barrier
	s_waitcnt lgkmcnt(0)
	s_setprio 1
	s_waitcnt lgkmcnt(0)
	v_mfma_f32_16x16x32_bf16 v[126:129], v[150:153], v[166:169], v[126:129]
	v_mfma_f32_16x16x32_bf16 v[122:125], v[158:161], v[166:169], v[122:125]
	v_mfma_f32_16x16x32_bf16 v[110:113], v[150:153], v[174:177], v[110:113]
	v_mfma_f32_16x16x32_bf16 v[106:109], v[158:161], v[174:177], v[106:109]
	v_mfma_f32_16x16x32_bf16 v[94:97], v[150:153], v[182:185], v[94:97]
	v_mfma_f32_16x16x32_bf16 v[90:93], v[158:161], v[182:185], v[90:93]
	v_mfma_f32_16x16x32_bf16 v[78:81], v[150:153], v[190:193], v[78:81]
	v_mfma_f32_16x16x32_bf16 v[74:77], v[158:161], v[190:193], v[74:77]
	v_mfma_f32_16x16x32_bf16 v[126:129], v[154:157], v[170:173], v[126:129]
	v_mfma_f32_16x16x32_bf16 v[122:125], v[162:165], v[170:173], v[122:125]
	v_mfma_f32_16x16x32_bf16 v[110:113], v[154:157], v[178:181], v[110:113]
	v_mfma_f32_16x16x32_bf16 v[106:109], v[162:165], v[178:181], v[106:109]
	v_mfma_f32_16x16x32_bf16 v[94:97], v[154:157], v[186:189], v[94:97]
	v_mfma_f32_16x16x32_bf16 v[90:93], v[162:165], v[186:189], v[90:93]
	v_mfma_f32_16x16x32_bf16 v[78:81], v[154:157], v[198:201], v[78:81]
	v_mfma_f32_16x16x32_bf16 v[74:77], v[162:165], v[198:201], v[74:77]
	s_setprio 0
	s_barrier
	s_add_i32 s58, 0, 0x1c040
	s_add_i32 s59, s96, s65
	v_add_u32_e32 v142, s58, v145
	v_lshl_add_u64 v[196:197], v[196:197], 0, s[10:11]
	s_mov_b32 m0, s59
	ds_read_b128 v[202:205], v142
	ds_read_b128 v[206:209], v142 offset:1024
	ds_read_b128 v[210:213], v142 offset:2048
	ds_read_b128 v[214:217], v142 offset:3072
	global_load_lds_dwordx4 v[196:197], off
	v_lshl_add_u64 v[196:197], v[218:219], 0, s[10:11]
	s_add_i32 m0, s59, 0x2000
	s_nop 0
	global_load_lds_dwordx4 v[196:197], off
	s_barrier
	s_waitcnt lgkmcnt(0)
	s_setprio 1
	s_waitcnt lgkmcnt(0)
	v_mfma_f32_16x16x32_bf16 v[118:121], v[202:205], v[166:169], v[118:121]
	v_mfma_f32_16x16x32_bf16 v[114:117], v[210:213], v[166:169], v[114:117]
	v_mfma_f32_16x16x32_bf16 v[102:105], v[202:205], v[174:177], v[102:105]
	v_mfma_f32_16x16x32_bf16 v[98:101], v[210:213], v[174:177], v[98:101]
	v_mfma_f32_16x16x32_bf16 v[86:89], v[202:205], v[182:185], v[86:89]
	v_mfma_f32_16x16x32_bf16 v[82:85], v[210:213], v[182:185], v[82:85]
	v_mfma_f32_16x16x32_bf16 v[70:73], v[202:205], v[190:193], v[70:73]
	v_mfma_f32_16x16x32_bf16 v[66:69], v[210:213], v[190:193], v[66:69]
	v_mfma_f32_16x16x32_bf16 v[118:121], v[206:209], v[170:173], v[118:121]
	v_mfma_f32_16x16x32_bf16 v[114:117], v[214:217], v[170:173], v[114:117]
	v_mfma_f32_16x16x32_bf16 v[102:105], v[206:209], v[178:181], v[102:105]
	v_mfma_f32_16x16x32_bf16 v[98:101], v[214:217], v[178:181], v[98:101]
	v_mfma_f32_16x16x32_bf16 v[86:89], v[206:209], v[186:189], v[86:89]
	v_mfma_f32_16x16x32_bf16 v[82:85], v[214:217], v[186:189], v[82:85]
	v_mfma_f32_16x16x32_bf16 v[70:73], v[206:209], v[198:201], v[70:73]
	v_mfma_f32_16x16x32_bf16 v[66:69], v[214:217], v[198:201], v[66:69]
	s_setprio 0
	s_mov_b32 m0, s69
	v_lshl_add_u64 v[196:197], v[222:223], 0, s[10:11]
	s_barrier
	ds_read_b128 v[166:169], v149 offset:49216
	ds_read_b128 v[170:173], v149 offset:50240
	ds_read_b128 v[174:177], v149 offset:51264
	ds_read_b128 v[178:181], v149 offset:52288
	ds_read_b128 v[182:185], v149 offset:53312
	ds_read_b128 v[186:189], v149 offset:54336
	ds_read_b128 v[190:193], v149 offset:55360
	ds_read_b128 v[198:201], v149 offset:56384
	global_load_lds_dwordx4 v[196:197], off
	v_lshl_add_u64 v[196:197], v[224:225], 0, s[10:11]
	s_mov_b32 m0, s70
	s_nop 0
	global_load_lds_dwordx4 v[196:197], off
	s_barrier
	s_waitcnt lgkmcnt(0)
	s_setprio 1
	s_waitcnt lgkmcnt(0)
	v_mfma_f32_16x16x32_bf16 v[62:65], v[150:153], v[166:169], v[62:65]
	v_mfma_f32_16x16x32_bf16 v[58:61], v[158:161], v[166:169], v[58:61]
	v_mfma_f32_16x16x32_bf16 v[50:53], v[150:153], v[174:177], v[50:53]
	v_mfma_f32_16x16x32_bf16 v[42:45], v[158:161], v[174:177], v[42:45]
	v_mfma_f32_16x16x32_bf16 v[34:37], v[150:153], v[182:185], v[34:37]
	v_mfma_f32_16x16x32_bf16 v[26:29], v[158:161], v[182:185], v[26:29]
	v_mfma_f32_16x16x32_bf16 v[18:21], v[150:153], v[190:193], v[18:21]
	v_mfma_f32_16x16x32_bf16 v[10:13], v[158:161], v[190:193], v[10:13]
	v_mfma_f32_16x16x32_bf16 v[62:65], v[154:157], v[170:173], v[62:65]
	v_mfma_f32_16x16x32_bf16 v[58:61], v[162:165], v[170:173], v[58:61]
	v_mfma_f32_16x16x32_bf16 v[50:53], v[154:157], v[178:181], v[50:53]
	v_mfma_f32_16x16x32_bf16 v[42:45], v[162:165], v[178:181], v[42:45]
	v_mfma_f32_16x16x32_bf16 v[34:37], v[154:157], v[186:189], v[34:37]
	v_mfma_f32_16x16x32_bf16 v[26:29], v[162:165], v[186:189], v[26:29]
	v_mfma_f32_16x16x32_bf16 v[18:21], v[154:157], v[198:201], v[18:21]
	v_mfma_f32_16x16x32_bf16 v[10:13], v[162:165], v[198:201], v[10:13]
	s_setprio 0
	s_barrier
	s_add_u32 s56, s56, 0x40080
	s_addc_u32 s57, s57, 0
	s_add_i32 s58, s58, s65
	v_lshl_add_u64 v[150:151], s[56:57], 0, v[132:133]
	s_mov_b32 m0, s58
	s_nop 0
	global_load_lds_dwordx4 v[150:151], off
	v_lshl_add_u64 v[150:151], s[56:57], 0, v[136:137]
	s_add_i32 m0, s58, 0x2000
	s_nop 0
	global_load_lds_dwordx4 v[150:151], off
	s_waitcnt vmcnt(6)
	s_barrier
	s_setprio 1
	v_mfma_f32_16x16x32_bf16 v[54:57], v[202:205], v[166:169], v[54:57]
	v_mfma_f32_16x16x32_bf16 v[46:49], v[210:213], v[166:169], v[46:49]
	v_mfma_f32_16x16x32_bf16 v[38:41], v[202:205], v[174:177], v[38:41]
	v_mfma_f32_16x16x32_bf16 v[30:33], v[210:213], v[174:177], v[30:33]
	v_mfma_f32_16x16x32_bf16 v[22:25], v[202:205], v[182:185], v[22:25]
	v_mfma_f32_16x16x32_bf16 v[14:17], v[210:213], v[182:185], v[14:17]
	v_mfma_f32_16x16x32_bf16 v[6:9], v[202:205], v[190:193], v[6:9]
	v_mfma_f32_16x16x32_bf16 v[2:5], v[210:213], v[190:193], v[2:5]
	v_mfma_f32_16x16x32_bf16 v[54:57], v[206:209], v[170:173], v[54:57]
	v_mfma_f32_16x16x32_bf16 v[46:49], v[214:217], v[170:173], v[46:49]
	v_mfma_f32_16x16x32_bf16 v[38:41], v[206:209], v[178:181], v[38:41]
	v_mfma_f32_16x16x32_bf16 v[30:33], v[214:217], v[178:181], v[30:33]
	v_mfma_f32_16x16x32_bf16 v[22:25], v[206:209], v[186:189], v[22:25]
	v_mfma_f32_16x16x32_bf16 v[14:17], v[214:217], v[186:189], v[14:17]
	v_mfma_f32_16x16x32_bf16 v[6:9], v[206:209], v[198:201], v[6:9]
	v_mfma_f32_16x16x32_bf16 v[2:5], v[214:217], v[198:201], v[2:5]
	s_setprio 0
	s_add_i32 s87, s87, 2
	s_add_u32 s35, s35, 0x100
	s_addc_u32 s86, s86, 0
	s_add_u32 s54, s54, 0x100
	s_addc_u32 s55, s55, 0
	s_cmp_gt_u32 s87, 13
	s_barrier
	s_cbranch_scc0 .LBB0_1841
	v_lshl_add_u32 v158, s38, 8, v143
	v_ashrrev_i32_e32 v159, 31, v158
	v_lshl_add_u64 v[160:161], v[158:159], 2, s[44:45]
	v_mov_b32_e32 v162, v240
	v_mov_b32_e32 v166, v241
	v_mov_b32_e32 v154, v242
	v_mov_b32_e32 v150, v243
	v_mov_b32_e32 v148, v244
	v_mov_b32_e32 v146, v245
	v_mov_b32_e32 v144, v246
	v_mov_b32_e32 v142, v247
	s_lshl_b32 s9, s52, 8
	s_and_b32 s9, s9, 0x300
	v_or_b32_e32 v164, 16, v158
	v_or_b32_e32 v156, 32, v158
	v_or_b32_e32 v152, 48, v158
	v_or_b32_e32 v151, s9, v147
	v_lshlrev_b64 v[158:159], 11, v[158:159]
	v_lshlrev_b32_e32 v194, 1, v151
	v_ashrrev_i32_e32 v165, 31, v164
	v_ashrrev_i32_e32 v157, 31, v156
	v_ashrrev_i32_e32 v153, 31, v152
	s_mov_b32 s9, 0x40000
	s_mov_b64 s[14:15], 0x40000
	s_mov_b32 s52, s34
	s_mov_b32 s38, s30
	s_mov_b64 s[54:55], s[50:51]
	s_mov_b64 s[56:57], s[48:49]
	s_movk_i32 s97, 0x3000
	s_nop 0
	v_pk_mul_f32 v[78:79], v[78:79], v[150:151] op_sel_hi:[1,0]
	v_pk_mul_f32 v[126:127], v[126:127], v[162:163] op_sel_hi:[1,0]
	v_pk_mul_f32 v[122:123], v[122:123], v[162:163] op_sel_hi:[1,0]
	v_pk_mul_f32 v[160:161], v[124:125], v[162:163] op_sel_hi:[1,0]
	v_cvt_pk_bf16_f32 v124, v126, v127
	v_cvt_pk_bf16_f32 v126, v122, v123
	v_lshl_add_u64 v[122:123], s[42:43], 0, v[158:159]
	v_pk_mul_f32 v[128:129], v[128:129], v[162:163] op_sel_hi:[1,0]
	v_lshl_add_u64 v[122:123], v[122:123], 0, v[194:195]
	v_cvt_pk_bf16_f32 v125, v128, v129
	v_cvt_pk_bf16_f32 v127, v160, v161
	global_store_dwordx4 v[122:123], v[124:127], off
	v_pk_mul_f32 v[120:121], v[120:121], v[162:163] op_sel_hi:[1,0]
	v_pk_mul_f32 v[118:119], v[118:119], v[162:163] op_sel_hi:[1,0]
	v_pk_mul_f32 v[124:125], v[116:117], v[162:163] op_sel_hi:[1,0]
	v_pk_mul_f32 v[116:117], v[114:115], v[162:163] op_sel_hi:[1,0]
	v_cvt_pk_bf16_f32 v114, v118, v119
	v_cvt_pk_bf16_f32 v115, v120, v121
	v_pk_mul_f32 v[110:111], v[110:111], v[166:167] op_sel_hi:[1,0]
	v_cvt_pk_bf16_f32 v116, v116, v117
	v_cvt_pk_bf16_f32 v117, v124, v125
	global_store_dwordx4 v[122:123], v[114:117], off offset:256
	v_pk_mul_f32 v[112:113], v[112:113], v[166:167] op_sel_hi:[1,0]
	v_pk_mul_f32 v[104:105], v[104:105], v[166:167] op_sel_hi:[1,0]
	v_lshlrev_b64 v[114:115], 11, v[164:165]
	v_pk_mul_f32 v[116:117], v[108:109], v[166:167] op_sel_hi:[1,0]
	v_pk_mul_f32 v[108:109], v[106:107], v[166:167] op_sel_hi:[1,0]
	v_cvt_pk_bf16_f32 v106, v110, v111
	v_lshl_add_u64 v[110:111], s[42:43], 0, v[114:115]
	v_cvt_pk_bf16_f32 v107, v112, v113
	v_lshl_add_u64 v[110:111], v[110:111], 0, v[194:195]
	v_cvt_pk_bf16_f32 v108, v108, v109
	v_cvt_pk_bf16_f32 v109, v116, v117
	global_store_dwordx4 v[110:111], v[106:109], off
	v_pk_mul_f32 v[102:103], v[102:103], v[166:167] op_sel_hi:[1,0]
	v_pk_mul_f32 v[94:95], v[94:95], v[154:155] op_sel_hi:[1,0]
	v_pk_mul_f32 v[106:107], v[100:101], v[166:167] op_sel_hi:[1,0]
	v_pk_mul_f32 v[100:101], v[98:99], v[166:167] op_sel_hi:[1,0]
	v_cvt_pk_bf16_f32 v98, v102, v103
	v_cvt_pk_bf16_f32 v99, v104, v105
	v_pk_mul_f32 v[96:97], v[96:97], v[154:155] op_sel_hi:[1,0]
	v_cvt_pk_bf16_f32 v100, v100, v101
	v_cvt_pk_bf16_f32 v101, v106, v107
	global_store_dwordx4 v[110:111], v[98:101], off offset:256
	v_pk_mul_f32 v[88:89], v[88:89], v[154:155] op_sel_hi:[1,0]
	v_pk_mul_f32 v[86:87], v[86:87], v[154:155] op_sel_hi:[1,0]
	v_lshlrev_b64 v[98:99], 11, v[156:157]
	v_pk_mul_f32 v[100:101], v[92:93], v[154:155] op_sel_hi:[1,0]
	v_pk_mul_f32 v[92:93], v[90:91], v[154:155] op_sel_hi:[1,0]
	v_cvt_pk_bf16_f32 v90, v94, v95
	v_lshl_add_u64 v[94:95], s[42:43], 0, v[98:99]
	v_cvt_pk_bf16_f32 v91, v96, v97
	v_lshl_add_u64 v[94:95], v[94:95], 0, v[194:195]
	v_cvt_pk_bf16_f32 v92, v92, v93
	v_cvt_pk_bf16_f32 v93, v100, v101
	global_store_dwordx4 v[94:95], v[90:93], off
	v_pk_mul_f32 v[80:81], v[80:81], v[150:151] op_sel_hi:[1,0]
	v_pk_mul_f32 v[72:73], v[72:73], v[150:151] op_sel_hi:[1,0]
	v_pk_mul_f32 v[90:91], v[84:85], v[154:155] op_sel_hi:[1,0]
	v_pk_mul_f32 v[84:85], v[82:83], v[154:155] op_sel_hi:[1,0]
	v_cvt_pk_bf16_f32 v82, v86, v87
	v_cvt_pk_bf16_f32 v83, v88, v89
	v_pk_mul_f32 v[70:71], v[70:71], v[150:151] op_sel_hi:[1,0]
	v_cvt_pk_bf16_f32 v84, v84, v85
	v_cvt_pk_bf16_f32 v85, v90, v91
	global_store_dwordx4 v[94:95], v[82:85], off offset:256
	v_pk_mul_f32 v[64:65], v[64:65], v[148:149] op_sel_hi:[1,0]
	v_pk_mul_f32 v[62:63], v[62:63], v[148:149] op_sel_hi:[1,0]
	v_lshlrev_b64 v[82:83], 11, v[152:153]
	v_pk_mul_f32 v[84:85], v[76:77], v[150:151] op_sel_hi:[1,0]
	v_pk_mul_f32 v[76:77], v[74:75], v[150:151] op_sel_hi:[1,0]
	v_cvt_pk_bf16_f32 v74, v78, v79
	v_lshl_add_u64 v[78:79], s[42:43], 0, v[82:83]
	v_cvt_pk_bf16_f32 v75, v80, v81
	v_lshl_add_u64 v[78:79], v[78:79], 0, v[194:195]
	v_cvt_pk_bf16_f32 v76, v76, v77
	v_cvt_pk_bf16_f32 v77, v84, v85
	global_store_dwordx4 v[78:79], v[74:77], off
	v_pk_mul_f32 v[56:57], v[56:57], v[148:149] op_sel_hi:[1,0]
	v_pk_mul_f32 v[54:55], v[54:55], v[148:149] op_sel_hi:[1,0]
	v_pk_mul_f32 v[74:75], v[68:69], v[150:151] op_sel_hi:[1,0]
	v_pk_mul_f32 v[68:69], v[66:67], v[150:151] op_sel_hi:[1,0]
	v_cvt_pk_bf16_f32 v66, v70, v71
	v_cvt_pk_bf16_f32 v67, v72, v73
	v_pk_mul_f32 v[40:41], v[40:41], v[146:147] op_sel_hi:[1,0]
	v_cvt_pk_bf16_f32 v68, v68, v69
	v_cvt_pk_bf16_f32 v69, v74, v75
	global_store_dwordx4 v[78:79], v[66:69], off offset:256
	v_pk_mul_f32 v[38:39], v[38:39], v[146:147] op_sel_hi:[1,0]
	v_pk_mul_f32 v[24:25], v[24:25], v[144:145] op_sel_hi:[1,0]
	v_pk_mul_f32 v[66:67], v[60:61], v[148:149] op_sel_hi:[1,0]
	v_pk_mul_f32 v[60:61], v[58:59], v[148:149] op_sel_hi:[1,0]
	v_cvt_pk_bf16_f32 v59, v64, v65
	v_add_co_u32_e32 v64, vcc, s9, v122
	v_cvt_pk_bf16_f32 v58, v62, v63
	v_cvt_pk_bf16_f32 v60, v60, v61
	v_cvt_pk_bf16_f32 v61, v66, v67
	v_lshl_add_u64 v[62:63], v[122:123], 0, s[14:15]
	s_nop 0
	v_addc_co_u32_e32 v65, vcc, 0, v123, vcc
	global_store_dwordx4 v[64:65], v[58:61], off
	s_mov_b32 s9, 0x48000
	s_mov_b64 s[14:15], 0x48000
	v_pk_mul_f32 v[58:59], v[48:49], v[148:149] op_sel_hi:[1,0]
	v_pk_mul_f32 v[48:49], v[46:47], v[148:149] op_sel_hi:[1,0]
	v_cvt_pk_bf16_f32 v46, v54, v55
	v_cvt_pk_bf16_f32 v47, v56, v57
	v_pk_mul_f32 v[22:23], v[22:23], v[144:145] op_sel_hi:[1,0]
	v_cvt_pk_bf16_f32 v48, v48, v49
	v_cvt_pk_bf16_f32 v49, v58, v59
	global_store_dwordx4 v[62:63], v[46:49], off offset:256
	v_pk_mul_f32 v[8:9], v[8:9], v[142:143] op_sel_hi:[1,0]
	v_pk_mul_f32 v[6:7], v[6:7], v[142:143] op_sel_hi:[1,0]
	v_pk_mul_f32 v[48:49], v[50:51], v[146:147] op_sel_hi:[1,0]
	v_pk_mul_f32 v[50:51], v[44:45], v[146:147] op_sel_hi:[1,0]
	v_pk_mul_f32 v[44:45], v[42:43], v[146:147] op_sel_hi:[1,0]
	v_cvt_pk_bf16_f32 v42, v48, v49
	v_add_co_u32_e32 v48, vcc, s9, v122
	v_pk_mul_f32 v[46:47], v[52:53], v[146:147] op_sel_hi:[1,0]
	s_nop 0
	v_addc_co_u32_e32 v49, vcc, 0, v123, vcc
	v_cvt_pk_bf16_f32 v43, v46, v47
	v_cvt_pk_bf16_f32 v44, v44, v45
	v_cvt_pk_bf16_f32 v45, v50, v51
	global_store_dwordx4 v[48:49], v[42:45], off
	v_lshl_add_u64 v[46:47], v[122:123], 0, s[14:15]
	s_mov_b32 s9, 0x50000
	v_pk_mul_f32 v[42:43], v[32:33], v[146:147] op_sel_hi:[1,0]
	v_pk_mul_f32 v[32:33], v[30:31], v[146:147] op_sel_hi:[1,0]
	v_cvt_pk_bf16_f32 v30, v38, v39
	v_cvt_pk_bf16_f32 v31, v40, v41
	s_mov_b64 s[14:15], 0x50000
	v_cvt_pk_bf16_f32 v32, v32, v33
	v_cvt_pk_bf16_f32 v33, v42, v43
	global_store_dwordx4 v[46:47], v[30:33], off offset:256
	s_nop 1
	v_pk_mul_f32 v[32:33], v[34:35], v[144:145] op_sel_hi:[1,0]
	v_pk_mul_f32 v[34:35], v[28:29], v[144:145] op_sel_hi:[1,0]
	v_pk_mul_f32 v[28:29], v[26:27], v[144:145] op_sel_hi:[1,0]
	v_cvt_pk_bf16_f32 v26, v32, v33
	v_add_co_u32_e32 v32, vcc, s9, v122
	v_pk_mul_f32 v[30:31], v[36:37], v[144:145] op_sel_hi:[1,0]
	s_nop 0
	v_addc_co_u32_e32 v33, vcc, 0, v123, vcc
	v_cvt_pk_bf16_f32 v27, v30, v31
	v_cvt_pk_bf16_f32 v28, v28, v29
	v_cvt_pk_bf16_f32 v29, v34, v35
	global_store_dwordx4 v[32:33], v[26:29], off
	v_lshl_add_u64 v[30:31], v[122:123], 0, s[14:15]
	s_mov_b32 s9, 0x58000
	v_pk_mul_f32 v[26:27], v[16:17], v[144:145] op_sel_hi:[1,0]
	v_pk_mul_f32 v[16:17], v[14:15], v[144:145] op_sel_hi:[1,0]
	v_cvt_pk_bf16_f32 v14, v22, v23
	v_cvt_pk_bf16_f32 v15, v24, v25
	s_mov_b64 s[14:15], 0x58000
	v_cvt_pk_bf16_f32 v16, v16, v17
	v_cvt_pk_bf16_f32 v17, v26, v27
	global_store_dwordx4 v[30:31], v[14:17], off offset:256
	s_nop 1
	v_pk_mul_f32 v[16:17], v[18:19], v[142:143] op_sel_hi:[1,0]
	v_pk_mul_f32 v[18:19], v[12:13], v[142:143] op_sel_hi:[1,0]
	v_pk_mul_f32 v[12:13], v[10:11], v[142:143] op_sel_hi:[1,0]
	v_cvt_pk_bf16_f32 v10, v16, v17
	v_add_co_u32_e32 v16, vcc, s9, v122
	v_pk_mul_f32 v[14:15], v[20:21], v[142:143] op_sel_hi:[1,0]
	s_nop 0
	v_addc_co_u32_e32 v17, vcc, 0, v123, vcc
	v_cvt_pk_bf16_f32 v11, v14, v15
	v_cvt_pk_bf16_f32 v12, v12, v13
	v_cvt_pk_bf16_f32 v13, v18, v19
	v_lshl_add_u64 v[14:15], v[122:123], 0, s[14:15]
	global_store_dwordx4 v[16:17], v[10:13], off
	s_and_b64 vcc, exec, s[46:47]
	s_nop 0
	v_pk_mul_f32 v[10:11], v[4:5], v[142:143] op_sel_hi:[1,0]
	v_pk_mul_f32 v[4:5], v[2:3], v[142:143] op_sel_hi:[1,0]
	v_cvt_pk_bf16_f32 v2, v6, v7
	v_cvt_pk_bf16_f32 v3, v8, v9
	s_nop 0
	v_cvt_pk_bf16_f32 v4, v4, v5
	v_cvt_pk_bf16_f32 v5, v10, v11
	global_store_dwordx4 v[14:15], v[2:5], off offset:256
	s_cbranch_vccz .LBB0_1835
	s_waitcnt vmcnt(0)
	s_cmpk_gt_u32 s62, 0xff
	s_cbranch_scc1 .LBB0_1845
	s_barrier
